# strategy 1 on LDS waits: inverse-FFT pass ds_reads issued one segment ahead into spare registers (counted by position, waits unchanged)
# baseline (speedup 1.0000x reference)
.LBB0_776:
	v_add_u32_e32 v38, s85, v4
	v_and_b32_e32 v38, 0xffffffc0, v38
	v_lshlrev_b32_e32 v102, 3, v38
	v_add3_u32 v38, v5, v38, v102
	ds_read2_b64 v[102:105], v38 offset1:9
	s_waitcnt lgkmcnt(0)
	ds_read2_b64 v[230:233], v38 offset0:18 offset1:27
	v_pk_mul_f32 v[106:107], v[104:105], v[2:3] op_sel_hi:[1,0]
	s_addk_i32 s85, 0x1000
	v_pk_fma_f32 v[108:109], v[104:105], v[2:3], v[106:107] op_sel:[1,1,0] op_sel_hi:[0,1,1] neg_lo:[1,0,0]
	v_pk_mul_f32 v[104:105], v[2:3], v[2:3] op_sel_hi:[1,0]
	s_cmpk_lg_i32 s85, 0x4000
	v_pk_fma_f32 v[110:111], v[2:3], v[2:3], v[104:105] op_sel:[1,1,0] op_sel_hi:[0,1,1] neg_lo:[1,0,0]
	s_waitcnt lgkmcnt(0)
	ds_read2_b64 v[234:237], v38 offset0:36 offset1:45
	v_pk_mul_f32 v[112:113], v[230:231], v[110:111] op_sel_hi:[1,0]
	v_pk_fma_f32 v[112:113], v[230:231], v[110:111], v[112:113] op_sel:[1,1,0] op_sel_hi:[0,1,1] neg_lo:[1,0,0]
	v_pk_mul_f32 v[104:105], v[110:111], v[2:3] op_sel_hi:[1,0]
	v_pk_fma_f32 v[104:105], v[110:111], v[2:3], v[104:105] op_sel:[1,1,0] op_sel_hi:[0,1,1] neg_lo:[1,0,0]
	v_pk_mul_f32 v[110:111], v[232:233], v[104:105] op_sel_hi:[1,0]
	v_pk_fma_f32 v[110:111], v[232:233], v[104:105], v[110:111] op_sel:[1,1,0] op_sel_hi:[0,1,1] neg_lo:[1,0,0]
	v_pk_mul_f32 v[106:107], v[104:105], v[2:3] op_sel_hi:[1,0]
	v_pk_fma_f32 v[114:115], v[104:105], v[2:3], v[106:107] op_sel:[1,1,0] op_sel_hi:[0,1,1] neg_lo:[1,0,0]
	s_waitcnt lgkmcnt(0)
	ds_read2_b64 v[230:233], v38 offset0:54 offset1:63
	v_pk_mul_f32 v[116:117], v[234:235], v[114:115] op_sel_hi:[1,0]
	v_pk_fma_f32 v[116:117], v[234:235], v[114:115], v[116:117] op_sel:[1,1,0] op_sel_hi:[0,1,1] neg_lo:[1,0,0]
	v_pk_mul_f32 v[104:105], v[114:115], v[2:3] op_sel_hi:[1,0]
	v_pk_fma_f32 v[104:105], v[114:115], v[2:3], v[104:105] op_sel:[1,1,0] op_sel_hi:[0,1,1] neg_lo:[1,0,0]
	v_pk_mul_f32 v[114:115], v[236:237], v[104:105] op_sel_hi:[1,0]
	v_pk_fma_f32 v[114:115], v[236:237], v[104:105], v[114:115] op_sel:[1,1,0] op_sel_hi:[0,1,1] neg_lo:[1,0,0]
	v_pk_mul_f32 v[106:107], v[104:105], v[2:3] op_sel_hi:[1,0]
	v_pk_fma_f32 v[118:119], v[104:105], v[2:3], v[106:107] op_sel:[1,1,0] op_sel_hi:[0,1,1] neg_lo:[1,0,0]
	s_waitcnt lgkmcnt(0)
	v_pk_mul_f32 v[120:121], v[230:231], v[118:119] op_sel_hi:[1,0]
	v_pk_fma_f32 v[104:105], v[230:231], v[118:119], v[120:121] op_sel:[1,1,0] op_sel_hi:[0,1,1] neg_lo:[1,0,0]
	v_pk_mul_f32 v[120:121], v[118:119], v[2:3] op_sel_hi:[1,0]
	v_pk_fma_f32 v[118:119], v[118:119], v[2:3], v[120:121] op_sel:[1,1,0] op_sel_hi:[0,1,1] neg_lo:[1,0,0]
	v_pk_mul_f32 v[120:121], v[232:233], v[118:119] op_sel_hi:[1,0]
	v_pk_fma_f32 v[106:107], v[232:233], v[118:119], v[120:121] op_sel:[1,1,0] op_sel_hi:[0,1,1] neg_lo:[1,0,0]
	v_pk_add_f32 v[118:119], v[102:103], v[116:117]
	v_pk_add_f32 v[102:103], v[102:103], v[116:117] neg_lo:[0,1] neg_hi:[0,1]
	v_pk_add_f32 v[116:117], v[108:109], v[114:115]
	v_pk_add_f32 v[108:109], v[108:109], v[114:115] neg_lo:[0,1] neg_hi:[0,1]
	v_mov_b64_e32 v[114:115], s[6:7]
	v_pk_mul_f32 v[120:121], v[108:109], v[114:115] op_sel_hi:[1,0]
	v_pk_fma_f32 v[108:109], v[108:109], v[114:115], v[120:121] op_sel:[1,1,0] op_sel_hi:[0,1,1] neg_lo:[1,0,0]
	v_pk_add_f32 v[114:115], v[112:113], v[104:105]
	v_pk_add_f32 v[104:105], v[112:113], v[104:105] op_sel:[1,1] op_sel_hi:[0,0] neg_lo:[1,0] neg_hi:[0,1]
	v_pk_add_f32 v[112:113], v[110:111], v[106:107]
	v_pk_add_f32 v[106:107], v[110:111], v[106:107] neg_lo:[0,1] neg_hi:[0,1]
	v_mov_b64_e32 v[110:111], s[14:15]
	v_pk_mul_f32 v[120:121], v[106:107], v[110:111] op_sel_hi:[1,0]
	v_pk_fma_f32 v[106:107], v[106:107], v[110:111], v[120:121] op_sel:[1,1,0] op_sel_hi:[0,1,1] neg_lo:[1,0,0]
	v_pk_add_f32 v[110:111], v[118:119], v[114:115]
	v_pk_add_f32 v[114:115], v[118:119], v[114:115] neg_lo:[0,1] neg_hi:[0,1]
	v_pk_add_f32 v[118:119], v[116:117], v[112:113]
	v_pk_add_f32 v[112:113], v[116:117], v[112:113] op_sel:[1,1] op_sel_hi:[0,0] neg_lo:[1,0] neg_hi:[0,1]
	v_pk_add_f32 v[116:117], v[102:103], v[104:105]
	v_pk_add_f32 v[102:103], v[102:103], v[104:105] neg_lo:[0,1] neg_hi:[0,1]
	v_pk_add_f32 v[104:105], v[108:109], v[106:107]
	v_pk_add_f32 v[106:107], v[108:109], v[106:107] op_sel:[1,1] op_sel_hi:[0,0] neg_lo:[1,0] neg_hi:[0,1]
	v_pk_add_f32 v[108:109], v[110:111], v[118:119]
	v_pk_add_f32 v[110:111], v[110:111], v[118:119] neg_lo:[0,1] neg_hi:[0,1]
	v_pk_add_f32 v[118:119], v[114:115], v[112:113]
	v_pk_add_f32 v[112:113], v[114:115], v[112:113] neg_lo:[0,1] neg_hi:[0,1]
	v_pk_add_f32 v[114:115], v[116:117], v[104:105]
	v_pk_add_f32 v[104:105], v[116:117], v[104:105] neg_lo:[0,1] neg_hi:[0,1]
	v_pk_add_f32 v[116:117], v[102:103], v[106:107]
	v_pk_add_f32 v[102:103], v[102:103], v[106:107] neg_lo:[0,1] neg_hi:[0,1]
	ds_write2_b64 v38, v[108:109], v[114:115] offset1:9
	ds_write2_b64 v38, v[118:119], v[116:117] offset0:18 offset1:27
	ds_write2_b64 v38, v[110:111], v[104:105] offset0:36 offset1:45
	ds_write2_b64 v38, v[112:113], v[102:103] offset0:54 offset1:63
	s_cbranch_scc1 .LBB0_776
	v_mov_b32_e32 v4, v204
	s_waitcnt lgkmcnt(0)
	s_barrier
	s_mov_b32 s85, 0
	v_and_b32_e32 v38, 63, v4
	v_cvt_f32_ubyte0_e32 v2, v38
	v_mul_f32_e32 v3, 0x3a800000, v2
	v_cos_f32_e32 v2, v3
	v_sin_f32_e32 v3, v3
	v_lshlrev_b32_e32 v132, 4, v4
	s_mov_b64 s[86:87], -1
.LBB0_778:
	v_add_u32_e32 v4, s85, v132
	v_and_b32_e32 v4, 0xfffffc00, v4
	v_or_b32_e32 v5, v4, v38
	v_bitop3_b32 v4, v4, s97, v38 bitop3:0xc8
	v_lshlrev_b32_e32 v5, 3, v5
	v_add3_u32 v133, 0, v4, v5
	ds_read2_b64 v[102:105], v133 offset1:72
	s_waitcnt lgkmcnt(0)
	v_pk_mul_f32 v[4:5], v[104:105], v[2:3] op_sel_hi:[1,0]
	v_add_u32_e32 v134, 0x800, v133
	v_pk_fma_f32 v[130:131], v[104:105], v[2:3], v[4:5] op_sel:[1,1,0] op_sel_hi:[0,1,1] neg_lo:[1,0,0]
	v_pk_mul_f32 v[4:5], v[2:3], v[2:3] op_sel_hi:[1,0]
	ds_read2_b64 v[104:107], v133 offset0:144 offset1:216
	v_pk_fma_f32 v[4:5], v[2:3], v[2:3], v[4:5] op_sel:[1,1,0] op_sel_hi:[0,1,1] neg_lo:[1,0,0]
	v_add_u32_e32 v135, 0x1000, v133
	s_waitcnt lgkmcnt(0)
	ds_read2_b64 v[230:233], v134 offset0:32 offset1:104
	v_pk_mul_f32 v[108:109], v[104:105], v[4:5] op_sel_hi:[1,0]
	v_add_u32_e32 v136, 0x1400, v133
	v_pk_fma_f32 v[120:121], v[104:105], v[4:5], v[108:109] op_sel:[1,1,0] op_sel_hi:[0,1,1] neg_lo:[1,0,0]
	v_pk_mul_f32 v[104:105], v[4:5], v[2:3] op_sel_hi:[1,0]
	v_add_u32_e32 v137, 0x1800, v133
	v_pk_fma_f32 v[4:5], v[4:5], v[2:3], v[104:105] op_sel:[1,1,0] op_sel_hi:[0,1,1] neg_lo:[1,0,0]
	v_add_u32_e32 v138, 0x1c00, v133
	v_pk_mul_f32 v[104:105], v[106:107], v[4:5] op_sel_hi:[1,0]
	s_movk_i32 s85, 0x2000
	v_pk_fma_f32 v[118:119], v[106:107], v[4:5], v[104:105] op_sel:[1,1,0] op_sel_hi:[0,1,1] neg_lo:[1,0,0]
	v_pk_mul_f32 v[104:105], v[4:5], v[2:3] op_sel_hi:[1,0]
	s_and_b64 vcc, exec, s[86:87]
	v_pk_fma_f32 v[4:5], v[4:5], v[2:3], v[104:105] op_sel:[1,1,0] op_sel_hi:[0,1,1] neg_lo:[1,0,0]
	s_waitcnt lgkmcnt(0)
	ds_read2_b64 v[234:237], v134 offset0:176 offset1:248
	v_pk_mul_f32 v[108:109], v[230:231], v[4:5] op_sel_hi:[1,0]
	s_mov_b64 s[86:87], 0
	v_pk_fma_f32 v[112:113], v[230:231], v[4:5], v[108:109] op_sel:[1,1,0] op_sel_hi:[0,1,1] neg_lo:[1,0,0]
	v_pk_mul_f32 v[104:105], v[4:5], v[2:3] op_sel_hi:[1,0]
	v_pk_fma_f32 v[4:5], v[4:5], v[2:3], v[104:105] op_sel:[1,1,0] op_sel_hi:[0,1,1] neg_lo:[1,0,0]
	v_pk_mul_f32 v[104:105], v[232:233], v[4:5] op_sel_hi:[1,0]
	v_pk_fma_f32 v[114:115], v[232:233], v[4:5], v[104:105] op_sel:[1,1,0] op_sel_hi:[0,1,1] neg_lo:[1,0,0]
	v_pk_mul_f32 v[104:105], v[4:5], v[2:3] op_sel_hi:[1,0]
	v_pk_fma_f32 v[4:5], v[4:5], v[2:3], v[104:105] op_sel:[1,1,0] op_sel_hi:[0,1,1] neg_lo:[1,0,0]
	s_waitcnt lgkmcnt(0)
	ds_read2_b64 v[230:233], v135 offset0:64 offset1:136
	v_pk_mul_f32 v[108:109], v[234:235], v[4:5] op_sel_hi:[1,0]
	v_pk_fma_f32 v[104:105], v[234:235], v[4:5], v[108:109] op_sel:[1,1,0] op_sel_hi:[0,1,1] neg_lo:[1,0,0]
	v_pk_mul_f32 v[108:109], v[4:5], v[2:3] op_sel_hi:[1,0]
	v_pk_fma_f32 v[108:109], v[4:5], v[2:3], v[108:109] op_sel:[1,1,0] op_sel_hi:[0,1,1] neg_lo:[1,0,0]
	v_pk_mul_f32 v[4:5], v[236:237], v[108:109] op_sel_hi:[1,0]
	v_pk_fma_f32 v[4:5], v[236:237], v[108:109], v[4:5] op_sel:[1,1,0] op_sel_hi:[0,1,1] neg_lo:[1,0,0]
	v_pk_mul_f32 v[106:107], v[108:109], v[2:3] op_sel_hi:[1,0]
	v_pk_fma_f32 v[110:111], v[108:109], v[2:3], v[106:107] op_sel:[1,1,0] op_sel_hi:[0,1,1] neg_lo:[1,0,0]
	s_waitcnt lgkmcnt(0)
	ds_read2_b64 v[234:237], v136 offset0:80 offset1:152
	v_pk_mul_f32 v[116:117], v[230:231], v[110:111] op_sel_hi:[1,0]
	v_pk_fma_f32 v[140:141], v[230:231], v[110:111], v[116:117] op_sel:[1,1,0] op_sel_hi:[0,1,1] neg_lo:[1,0,0]
	v_pk_mul_f32 v[106:107], v[110:111], v[2:3] op_sel_hi:[1,0]
	v_pk_fma_f32 v[106:107], v[110:111], v[2:3], v[106:107] op_sel:[1,1,0] op_sel_hi:[0,1,1] neg_lo:[1,0,0]
	v_pk_mul_f32 v[110:111], v[232:233], v[106:107] op_sel_hi:[1,0]
	v_pk_fma_f32 v[142:143], v[232:233], v[106:107], v[110:111] op_sel:[1,1,0] op_sel_hi:[0,1,1] neg_lo:[1,0,0]
	v_pk_mul_f32 v[108:109], v[106:107], v[2:3] op_sel_hi:[1,0]
	v_pk_fma_f32 v[110:111], v[106:107], v[2:3], v[108:109] op_sel:[1,1,0] op_sel_hi:[0,1,1] neg_lo:[1,0,0]
	s_waitcnt lgkmcnt(0)
	ds_read2_b64 v[230:233], v137 offset0:96 offset1:168
	v_pk_mul_f32 v[116:117], v[234:235], v[110:111] op_sel_hi:[1,0]
	v_pk_fma_f32 v[128:129], v[234:235], v[110:111], v[116:117] op_sel:[1,1,0] op_sel_hi:[0,1,1] neg_lo:[1,0,0]
	v_pk_mul_f32 v[106:107], v[110:111], v[2:3] op_sel_hi:[1,0]
	v_pk_fma_f32 v[106:107], v[110:111], v[2:3], v[106:107] op_sel:[1,1,0] op_sel_hi:[0,1,1] neg_lo:[1,0,0]
	v_pk_mul_f32 v[110:111], v[236:237], v[106:107] op_sel_hi:[1,0]
	v_pk_fma_f32 v[126:127], v[236:237], v[106:107], v[110:111] op_sel:[1,1,0] op_sel_hi:[0,1,1] neg_lo:[1,0,0]
	v_pk_mul_f32 v[108:109], v[106:107], v[2:3] op_sel_hi:[1,0]
	v_pk_fma_f32 v[110:111], v[106:107], v[2:3], v[108:109] op_sel:[1,1,0] op_sel_hi:[0,1,1] neg_lo:[1,0,0]
	s_waitcnt lgkmcnt(0)
	ds_read2_b64 v[234:237], v138 offset0:112 offset1:184
	v_pk_mul_f32 v[116:117], v[230:231], v[110:111] op_sel_hi:[1,0]
	v_pk_fma_f32 v[122:123], v[230:231], v[110:111], v[116:117] op_sel:[1,1,0] op_sel_hi:[0,1,1] neg_lo:[1,0,0]
	v_pk_mul_f32 v[106:107], v[110:111], v[2:3] op_sel_hi:[1,0]
	v_pk_fma_f32 v[106:107], v[110:111], v[2:3], v[106:107] op_sel:[1,1,0] op_sel_hi:[0,1,1] neg_lo:[1,0,0]
	v_pk_mul_f32 v[110:111], v[232:233], v[106:107] op_sel_hi:[1,0]
	v_pk_fma_f32 v[124:125], v[232:233], v[106:107], v[110:111] op_sel:[1,1,0] op_sel_hi:[0,1,1] neg_lo:[1,0,0]
	v_pk_mul_f32 v[108:109], v[106:107], v[2:3] op_sel_hi:[1,0]
	v_pk_fma_f32 v[110:111], v[106:107], v[2:3], v[108:109] op_sel:[1,1,0] op_sel_hi:[0,1,1] neg_lo:[1,0,0]
	s_waitcnt lgkmcnt(0)
	v_pk_mul_f32 v[116:117], v[234:235], v[110:111] op_sel_hi:[1,0]
	v_pk_fma_f32 v[116:117], v[234:235], v[110:111], v[116:117] op_sel:[1,1,0] op_sel_hi:[0,1,1] neg_lo:[1,0,0]
	v_pk_mul_f32 v[106:107], v[110:111], v[2:3] op_sel_hi:[1,0]
	v_pk_fma_f32 v[106:107], v[110:111], v[2:3], v[106:107] op_sel:[1,1,0] op_sel_hi:[0,1,1] neg_lo:[1,0,0]
	v_pk_mul_f32 v[110:111], v[236:237], v[106:107] op_sel_hi:[1,0]
	v_pk_fma_f32 v[110:111], v[236:237], v[106:107], v[110:111] op_sel:[1,1,0] op_sel_hi:[0,1,1] neg_lo:[1,0,0]
	v_pk_add_f32 v[106:107], v[102:103], v[140:141]
	v_pk_add_f32 v[102:103], v[102:103], v[140:141] neg_lo:[0,1] neg_hi:[0,1]
	v_pk_add_f32 v[108:109], v[130:131], v[142:143]
	v_pk_add_f32 v[130:131], v[130:131], v[142:143] neg_lo:[0,1] neg_hi:[0,1]
	v_mov_b64_e32 v[140:141], s[4:5]
	v_pk_mul_f32 v[142:143], v[130:131], v[140:141] op_sel_hi:[1,0]
	v_pk_fma_f32 v[130:131], v[130:131], v[140:141], v[142:143] op_sel:[1,1,0] op_sel_hi:[0,1,1] neg_lo:[1,0,0]
	v_pk_add_f32 v[140:141], v[120:121], v[128:129]
	v_pk_add_f32 v[120:121], v[120:121], v[128:129] neg_lo:[0,1] neg_hi:[0,1]
	v_mov_b64_e32 v[128:129], s[6:7]
	v_pk_mul_f32 v[142:143], v[120:121], v[128:129] op_sel_hi:[1,0]
	v_pk_fma_f32 v[120:121], v[120:121], v[128:129], v[142:143] op_sel:[1,1,0] op_sel_hi:[0,1,1] neg_lo:[1,0,0]
	v_pk_add_f32 v[142:143], v[118:119], v[126:127]
	v_pk_add_f32 v[118:119], v[118:119], v[126:127] neg_lo:[0,1] neg_hi:[0,1]
	v_mov_b64_e32 v[126:127], s[10:11]
	v_pk_mul_f32 v[144:145], v[118:119], v[126:127] op_sel_hi:[1,0]
	v_pk_fma_f32 v[118:119], v[118:119], v[126:127], v[144:145] op_sel:[1,1,0] op_sel_hi:[0,1,1] neg_lo:[1,0,0]
	v_pk_add_f32 v[126:127], v[112:113], v[122:123]
	v_pk_add_f32 v[112:113], v[112:113], v[122:123] op_sel:[1,1] op_sel_hi:[0,0] neg_lo:[1,0] neg_hi:[0,1]
	v_pk_add_f32 v[122:123], v[114:115], v[124:125]
	v_pk_add_f32 v[114:115], v[114:115], v[124:125] neg_lo:[0,1] neg_hi:[0,1]
	v_mov_b64_e32 v[124:125], s[12:13]
	v_pk_mul_f32 v[144:145], v[114:115], v[124:125] op_sel_hi:[1,0]
	v_pk_fma_f32 v[114:115], v[114:115], v[124:125], v[144:145] op_sel:[1,1,0] op_sel_hi:[0,1,1] neg_lo:[1,0,0]
	v_pk_add_f32 v[124:125], v[104:105], v[116:117]
	v_pk_add_f32 v[104:105], v[104:105], v[116:117] neg_lo:[0,1] neg_hi:[0,1]
	v_mov_b64_e32 v[116:117], s[14:15]
	v_pk_mul_f32 v[144:145], v[104:105], v[116:117] op_sel_hi:[1,0]
	v_pk_fma_f32 v[104:105], v[104:105], v[116:117], v[144:145] op_sel:[1,1,0] op_sel_hi:[0,1,1] neg_lo:[1,0,0]
	v_pk_add_f32 v[144:145], v[4:5], v[110:111]
	v_pk_add_f32 v[4:5], v[4:5], v[110:111] neg_lo:[0,1] neg_hi:[0,1]
	v_mov_b64_e32 v[110:111], s[16:17]
	v_pk_mul_f32 v[146:147], v[4:5], v[110:111] op_sel_hi:[1,0]
	v_pk_fma_f32 v[4:5], v[4:5], v[110:111], v[146:147] op_sel:[1,1,0] op_sel_hi:[0,1,1] neg_lo:[1,0,0]
	v_pk_add_f32 v[110:111], v[106:107], v[126:127]
	v_pk_add_f32 v[106:107], v[106:107], v[126:127] neg_lo:[0,1] neg_hi:[0,1]
	v_pk_add_f32 v[126:127], v[108:109], v[122:123]
	v_pk_add_f32 v[108:109], v[108:109], v[122:123] neg_lo:[0,1] neg_hi:[0,1]
	s_nop 0
	v_pk_mul_f32 v[122:123], v[108:109], v[128:129] op_sel_hi:[1,0]
	v_pk_fma_f32 v[108:109], v[108:109], v[128:129], v[122:123] op_sel:[1,1,0] op_sel_hi:[0,1,1] neg_lo:[1,0,0]
	v_pk_add_f32 v[122:123], v[140:141], v[124:125]
	v_pk_add_f32 v[124:125], v[140:141], v[124:125] op_sel:[1,1] op_sel_hi:[0,0] neg_lo:[1,0] neg_hi:[0,1]
	v_pk_add_f32 v[140:141], v[142:143], v[144:145]
	v_pk_add_f32 v[142:143], v[142:143], v[144:145] neg_lo:[0,1] neg_hi:[0,1]
	s_nop 0
	v_pk_mul_f32 v[144:145], v[142:143], v[116:117] op_sel_hi:[1,0]
	v_pk_fma_f32 v[142:143], v[142:143], v[116:117], v[144:145] op_sel:[1,1,0] op_sel_hi:[0,1,1] neg_lo:[1,0,0]
	v_pk_add_f32 v[144:145], v[102:103], v[112:113]
	v_pk_add_f32 v[102:103], v[102:103], v[112:113] neg_lo:[0,1] neg_hi:[0,1]
	v_pk_add_f32 v[112:113], v[130:131], v[114:115]
	v_pk_add_f32 v[114:115], v[130:131], v[114:115] neg_lo:[0,1] neg_hi:[0,1]
	s_nop 0
	v_pk_mul_f32 v[130:131], v[114:115], v[128:129] op_sel_hi:[1,0]
	v_pk_fma_f32 v[114:115], v[114:115], v[128:129], v[130:131] op_sel:[1,1,0] op_sel_hi:[0,1,1] neg_lo:[1,0,0]
	v_pk_add_f32 v[128:129], v[120:121], v[104:105]
	v_pk_add_f32 v[104:105], v[120:121], v[104:105] op_sel:[1,1] op_sel_hi:[0,0] neg_lo:[1,0] neg_hi:[0,1]
	v_pk_add_f32 v[120:121], v[118:119], v[4:5]
	v_pk_add_f32 v[4:5], v[118:119], v[4:5] neg_lo:[0,1] neg_hi:[0,1]
	v_pk_add_f32 v[130:131], v[144:145], v[128:129]
	v_pk_mul_f32 v[118:119], v[4:5], v[116:117] op_sel_hi:[1,0]
	v_pk_add_f32 v[128:129], v[144:145], v[128:129] neg_lo:[0,1] neg_hi:[0,1]
	v_pk_fma_f32 v[4:5], v[4:5], v[116:117], v[118:119] op_sel:[1,1,0] op_sel_hi:[0,1,1] neg_lo:[1,0,0]
	v_pk_add_f32 v[116:117], v[110:111], v[122:123]
	v_pk_add_f32 v[110:111], v[110:111], v[122:123] neg_lo:[0,1] neg_hi:[0,1]
	v_pk_add_f32 v[118:119], v[126:127], v[140:141]
	v_pk_add_f32 v[122:123], v[126:127], v[140:141] op_sel:[1,1] op_sel_hi:[0,0] neg_lo:[1,0] neg_hi:[0,1]
	v_pk_add_f32 v[126:127], v[106:107], v[124:125]
	v_pk_add_f32 v[106:107], v[106:107], v[124:125] neg_lo:[0,1] neg_hi:[0,1]
	v_pk_add_f32 v[124:125], v[108:109], v[142:143]
	v_pk_add_f32 v[108:109], v[108:109], v[142:143] op_sel:[1,1] op_sel_hi:[0,0] neg_lo:[1,0] neg_hi:[0,1]
	v_pk_add_f32 v[140:141], v[112:113], v[120:121]
	v_pk_add_f32 v[112:113], v[112:113], v[120:121] op_sel:[1,1] op_sel_hi:[0,0] neg_lo:[1,0] neg_hi:[0,1]
	v_pk_add_f32 v[120:121], v[102:103], v[104:105]
	v_pk_add_f32 v[102:103], v[102:103], v[104:105] neg_lo:[0,1] neg_hi:[0,1]
	v_pk_add_f32 v[104:105], v[114:115], v[4:5]
	v_pk_add_f32 v[4:5], v[114:115], v[4:5] op_sel:[1,1] op_sel_hi:[0,0] neg_lo:[1,0] neg_hi:[0,1]
	v_pk_add_f32 v[114:115], v[116:117], v[118:119]
	v_pk_add_f32 v[116:117], v[116:117], v[118:119] neg_lo:[0,1] neg_hi:[0,1]
	v_pk_add_f32 v[118:119], v[110:111], v[122:123]
	v_pk_add_f32 v[110:111], v[110:111], v[122:123] neg_lo:[0,1] neg_hi:[0,1]
	v_pk_add_f32 v[122:123], v[126:127], v[124:125]
	v_pk_add_f32 v[124:125], v[126:127], v[124:125] neg_lo:[0,1] neg_hi:[0,1]
	v_pk_add_f32 v[126:127], v[106:107], v[108:109]
	v_pk_add_f32 v[106:107], v[106:107], v[108:109] neg_lo:[0,1] neg_hi:[0,1]
	v_pk_add_f32 v[108:109], v[130:131], v[140:141]
	v_pk_add_f32 v[130:131], v[130:131], v[140:141] neg_lo:[0,1] neg_hi:[0,1]
	v_pk_add_f32 v[140:141], v[128:129], v[112:113]
	v_pk_add_f32 v[112:113], v[128:129], v[112:113] neg_lo:[0,1] neg_hi:[0,1]
	v_pk_add_f32 v[128:129], v[120:121], v[104:105]
	v_pk_add_f32 v[104:105], v[120:121], v[104:105] neg_lo:[0,1] neg_hi:[0,1]
	v_pk_add_f32 v[120:121], v[102:103], v[4:5]
	v_pk_add_f32 v[4:5], v[102:103], v[4:5] neg_lo:[0,1] neg_hi:[0,1]
	ds_write2_b64 v133, v[114:115], v[108:109] offset1:72
	ds_write2_b64 v133, v[122:123], v[128:129] offset0:144 offset1:216
	ds_write2_b64 v134, v[118:119], v[140:141] offset0:32 offset1:104
	ds_write2_b64 v134, v[126:127], v[120:121] offset0:176 offset1:248
	ds_write2_b64 v135, v[116:117], v[130:131] offset0:64 offset1:136
	ds_write2_b64 v136, v[124:125], v[104:105] offset0:80 offset1:152
	ds_write2_b64 v137, v[110:111], v[112:113] offset0:96 offset1:168
	ds_write2_b64 v138, v[106:107], v[4:5] offset0:112 offset1:184
	s_cbranch_vccnz .LBB0_778
	s_lshl_b32 s85, s83, 2
	s_add_i32 s85, s85, 0
	s_add_i32 s85, s85, 0x24400
	s_waitcnt lgkmcnt(0)
	s_barrier
	v_mov_b32_e32 v2, s85
	v_mov_b32_e32 v118, v204
	ds_read_b32 v38, v2
	s_ashr_i32 s85, s84, 31
	v_cvt_f32_i32_e32 v102, v118
	v_and_b32_e32 v2, -8, v118
	v_lshlrev_b32_e32 v119, 3, v118
	v_add3_u32 v116, 0, v2, v119
	v_mul_f32_e32 v102, 0x38800000, v102
	ds_read2st64_b64 v[2:5], v116 offset1:18
	v_cos_f32_e32 v106, v102
	v_sin_f32_e32 v107, v102
	s_waitcnt lgkmcnt(0)
	ds_read2st64_b64 v[230:233], v116 offset0:36 offset1:54
	v_pk_mul_f32 v[102:103], v[4:5], v[106:107] op_sel_hi:[1,0]
	v_add_u32_e32 v122, 0x12000, v116
	v_pk_fma_f32 v[4:5], v[4:5], v[106:107], v[102:103] op_sel:[1,1,0] op_sel_hi:[0,1,1] neg_lo:[1,0,0]
	v_pk_mul_f32 v[102:103], v[106:107], v[106:107] op_sel_hi:[1,0]
	v_add_u32_e32 v124, 0x14400, v116
	v_pk_fma_f32 v[108:109], v[106:107], v[106:107], v[102:103] op_sel:[1,1,0] op_sel_hi:[0,1,1] neg_lo:[1,0,0]
	s_waitcnt lgkmcnt(0)
	ds_read2st64_b64 v[234:237], v116 offset0:72 offset1:90
	v_pk_mul_f32 v[110:111], v[230:231], v[108:109] op_sel_hi:[1,0]
	v_add_u32_e32 v126, 0x16800, v116
	v_pk_fma_f32 v[102:103], v[230:231], v[108:109], v[110:111] op_sel:[1,1,0] op_sel_hi:[0,1,1] neg_lo:[1,0,0]
	v_pk_mul_f32 v[110:111], v[108:109], v[106:107] op_sel_hi:[1,0]
	v_add_u32_e32 v128, 0x18c00, v116
	v_pk_fma_f32 v[108:109], v[108:109], v[106:107], v[110:111] op_sel:[1,1,0] op_sel_hi:[0,1,1] neg_lo:[1,0,0]
	v_add_u32_e32 v130, 0x1b000, v116
	v_pk_mul_f32 v[110:111], v[232:233], v[108:109] op_sel_hi:[1,0]
	v_add_u32_e32 v132, 0x1d400, v116
	v_pk_fma_f32 v[104:105], v[232:233], v[108:109], v[110:111] op_sel:[1,1,0] op_sel_hi:[0,1,1] neg_lo:[1,0,0]
	v_pk_mul_f32 v[110:111], v[108:109], v[106:107] op_sel_hi:[1,0]
	v_add_u32_e32 v134, 0x1f800, v116
	v_pk_fma_f32 v[108:109], v[108:109], v[106:107], v[110:111] op_sel:[1,1,0] op_sel_hi:[0,1,1] neg_lo:[1,0,0]
	s_waitcnt lgkmcnt(0)
	ds_read2st64_b64 v[230:233], v116 offset0:108 offset1:126
	v_pk_mul_f32 v[114:115], v[234:235], v[108:109] op_sel_hi:[1,0]
	v_add_u32_e32 v136, 0x21c00, v116
	v_pk_fma_f32 v[110:111], v[234:235], v[108:109], v[114:115] op_sel:[1,1,0] op_sel_hi:[0,1,1] neg_lo:[1,0,0]
	v_pk_mul_f32 v[114:115], v[108:109], v[106:107] op_sel_hi:[1,0]
	s_lshl_b64 s[84:85], s[84:85], 16
	v_pk_fma_f32 v[108:109], v[108:109], v[106:107], v[114:115] op_sel:[1,1,0] op_sel_hi:[0,1,1] neg_lo:[1,0,0]
	s_add_u32 s84, s88, s84
	v_pk_mul_f32 v[114:115], v[236:237], v[108:109] op_sel_hi:[1,0]
	s_addc_u32 s85, s89, s85
	v_pk_fma_f32 v[112:113], v[236:237], v[108:109], v[114:115] op_sel:[1,1,0] op_sel_hi:[0,1,1] neg_lo:[1,0,0]
	v_pk_mul_f32 v[114:115], v[108:109], v[106:107] op_sel_hi:[1,0]
	s_add_i32 s83, s83, 1
	v_pk_fma_f32 v[108:109], v[108:109], v[106:107], v[114:115] op_sel:[1,1,0] op_sel_hi:[0,1,1] neg_lo:[1,0,0]
	s_waitcnt lgkmcnt(0)
	ds_read_b64 v[234:235], v122
	v_pk_mul_f32 v[120:121], v[230:231], v[108:109] op_sel_hi:[1,0]
	s_cmp_lg_u32 s83, 4
	v_pk_fma_f32 v[114:115], v[230:231], v[108:109], v[120:121] op_sel:[1,1,0] op_sel_hi:[0,1,1] neg_lo:[1,0,0]
	v_pk_mul_f32 v[120:121], v[108:109], v[106:107] op_sel_hi:[1,0]
	v_pk_fma_f32 v[108:109], v[108:109], v[106:107], v[120:121] op_sel:[1,1,0] op_sel_hi:[0,1,1] neg_lo:[1,0,0]
	v_pk_mul_f32 v[120:121], v[232:233], v[108:109] op_sel_hi:[1,0]
	v_pk_fma_f32 v[116:117], v[232:233], v[108:109], v[120:121] op_sel:[1,1,0] op_sel_hi:[0,1,1] neg_lo:[1,0,0]
	v_pk_mul_f32 v[120:121], v[108:109], v[106:107] op_sel_hi:[1,0]
	v_pk_fma_f32 v[120:121], v[108:109], v[106:107], v[120:121] op_sel:[1,1,0] op_sel_hi:[0,1,1] neg_lo:[1,0,0]
	s_waitcnt lgkmcnt(0)
	ds_read_b64 v[230:231], v124
	v_pk_mul_f32 v[122:123], v[234:235], v[120:121] op_sel_hi:[1,0]
	v_pk_fma_f32 v[108:109], v[234:235], v[120:121], v[122:123] op_sel:[1,1,0] op_sel_hi:[0,1,1] neg_lo:[1,0,0]
	v_pk_mul_f32 v[122:123], v[120:121], v[106:107] op_sel_hi:[1,0]
	v_pk_fma_f32 v[120:121], v[120:121], v[106:107], v[122:123] op_sel:[1,1,0] op_sel_hi:[0,1,1] neg_lo:[1,0,0]
	s_waitcnt lgkmcnt(0)
	ds_read_b64 v[232:233], v126
	v_pk_mul_f32 v[124:125], v[230:231], v[120:121] op_sel_hi:[1,0]
	v_pk_fma_f32 v[122:123], v[230:231], v[120:121], v[124:125] op_sel:[1,1,0] op_sel_hi:[0,1,1] neg_lo:[1,0,0]
	v_pk_mul_f32 v[124:125], v[120:121], v[106:107] op_sel_hi:[1,0]
	v_pk_fma_f32 v[120:121], v[120:121], v[106:107], v[124:125] op_sel:[1,1,0] op_sel_hi:[0,1,1] neg_lo:[1,0,0]
	s_waitcnt lgkmcnt(0)
	ds_read_b64 v[230:231], v128
	v_pk_mul_f32 v[126:127], v[232:233], v[120:121] op_sel_hi:[1,0]
	v_pk_fma_f32 v[124:125], v[232:233], v[120:121], v[126:127] op_sel:[1,1,0] op_sel_hi:[0,1,1] neg_lo:[1,0,0]
	v_pk_mul_f32 v[126:127], v[120:121], v[106:107] op_sel_hi:[1,0]
	v_pk_fma_f32 v[120:121], v[120:121], v[106:107], v[126:127] op_sel:[1,1,0] op_sel_hi:[0,1,1] neg_lo:[1,0,0]
	s_waitcnt lgkmcnt(0)
	ds_read_b64 v[232:233], v130
	v_pk_mul_f32 v[128:129], v[230:231], v[120:121] op_sel_hi:[1,0]
	v_pk_fma_f32 v[126:127], v[230:231], v[120:121], v[128:129] op_sel:[1,1,0] op_sel_hi:[0,1,1] neg_lo:[1,0,0]
	v_pk_mul_f32 v[128:129], v[120:121], v[106:107] op_sel_hi:[1,0]
	v_pk_fma_f32 v[120:121], v[120:121], v[106:107], v[128:129] op_sel:[1,1,0] op_sel_hi:[0,1,1] neg_lo:[1,0,0]
	s_waitcnt lgkmcnt(0)
	ds_read_b64 v[230:231], v132
	v_pk_mul_f32 v[130:131], v[232:233], v[120:121] op_sel_hi:[1,0]
	v_pk_add_f32 v[138:139], v[104:105], v[126:127]
	v_pk_fma_f32 v[128:129], v[232:233], v[120:121], v[130:131] op_sel:[1,1,0] op_sel_hi:[0,1,1] neg_lo:[1,0,0]
	v_pk_mul_f32 v[130:131], v[120:121], v[106:107] op_sel_hi:[1,0]
	v_pk_add_f32 v[104:105], v[104:105], v[126:127] neg_lo:[0,1] neg_hi:[0,1]
	v_pk_fma_f32 v[120:121], v[120:121], v[106:107], v[130:131] op_sel:[1,1,0] op_sel_hi:[0,1,1] neg_lo:[1,0,0]
	s_waitcnt lgkmcnt(0)
	v_pk_mul_f32 v[132:133], v[230:231], v[120:121] op_sel_hi:[1,0]
	v_pk_add_f32 v[140:141], v[110:111], v[128:129]
	v_pk_fma_f32 v[130:131], v[230:231], v[120:121], v[132:133] op_sel:[1,1,0] op_sel_hi:[0,1,1] neg_lo:[1,0,0]
	v_pk_mul_f32 v[132:133], v[120:121], v[106:107] op_sel_hi:[1,0]
	v_pk_add_f32 v[128:129], v[110:111], v[128:129] op_sel:[1,1] op_sel_hi:[0,0] neg_lo:[1,0] neg_hi:[0,1]
	v_mov_b64_e32 v[110:111], s[12:13]
	v_pk_fma_f32 v[120:121], v[120:121], v[106:107], v[132:133] op_sel:[1,1,0] op_sel_hi:[0,1,1] neg_lo:[1,0,0]
	ds_read_b64 v[132:133], v134
	s_waitcnt lgkmcnt(0)
	ds_read_b64 v[230:231], v136
	v_pk_mul_f32 v[134:135], v[132:133], v[120:121] op_sel_hi:[1,0]
	v_pk_add_f32 v[142:143], v[112:113], v[130:131]
	v_pk_fma_f32 v[132:133], v[132:133], v[120:121], v[134:135] op_sel:[1,1,0] op_sel_hi:[0,1,1] neg_lo:[1,0,0]
	v_pk_mul_f32 v[134:135], v[120:121], v[106:107] op_sel_hi:[1,0]
	v_pk_fma_f32 v[106:107], v[120:121], v[106:107], v[134:135] op_sel:[1,1,0] op_sel_hi:[0,1,1] neg_lo:[1,0,0]
	s_waitcnt lgkmcnt(0)
	v_pk_mul_f32 v[134:135], v[230:231], v[106:107] op_sel_hi:[1,0]
	v_pk_add_f32 v[136:137], v[4:5], v[122:123]
	v_pk_fma_f32 v[120:121], v[230:231], v[106:107], v[134:135] op_sel:[1,1,0] op_sel_hi:[0,1,1] neg_lo:[1,0,0]
	v_pk_add_f32 v[134:135], v[2:3], v[108:109]
	v_pk_add_f32 v[2:3], v[2:3], v[108:109] neg_lo:[0,1] neg_hi:[0,1]
	v_pk_add_f32 v[4:5], v[4:5], v[122:123] neg_lo:[0,1] neg_hi:[0,1]
	v_mov_b64_e32 v[106:107], s[4:5]
	v_pk_mul_f32 v[108:109], v[4:5], v[106:107] op_sel_hi:[1,0]
	v_pk_add_f32 v[122:123], v[102:103], v[124:125]
	v_pk_fma_f32 v[4:5], v[4:5], v[106:107], v[108:109] op_sel:[1,1,0] op_sel_hi:[0,1,1] neg_lo:[1,0,0]
	v_pk_add_f32 v[108:109], v[102:103], v[124:125] neg_lo:[0,1] neg_hi:[0,1]
	v_mov_b64_e32 v[102:103], s[6:7]
	v_pk_mul_f32 v[124:125], v[108:109], v[102:103] op_sel_hi:[1,0]
	v_pk_add_f32 v[144:145], v[114:115], v[132:133]
	v_pk_fma_f32 v[124:125], v[108:109], v[102:103], v[124:125] op_sel:[1,1,0] op_sel_hi:[0,1,1] neg_lo:[1,0,0]
	v_mov_b64_e32 v[108:109], s[10:11]
	v_pk_mul_f32 v[126:127], v[104:105], v[108:109] op_sel_hi:[1,0]
	v_pk_fma_f32 v[126:127], v[104:105], v[108:109], v[126:127] op_sel:[1,1,0] op_sel_hi:[0,1,1] neg_lo:[1,0,0]
	v_pk_add_f32 v[104:105], v[112:113], v[130:131] neg_lo:[0,1] neg_hi:[0,1]
	s_nop 0
	v_pk_mul_f32 v[112:113], v[104:105], v[110:111] op_sel_hi:[1,0]
	v_pk_fma_f32 v[130:131], v[104:105], v[110:111], v[112:113] op_sel:[1,1,0] op_sel_hi:[0,1,1] neg_lo:[1,0,0]
	v_pk_add_f32 v[112:113], v[114:115], v[132:133] neg_lo:[0,1] neg_hi:[0,1]
	v_mov_b64_e32 v[104:105], s[14:15]
	v_pk_mul_f32 v[114:115], v[112:113], v[104:105] op_sel_hi:[1,0]
	v_pk_add_f32 v[132:133], v[116:117], v[120:121]
	v_pk_fma_f32 v[114:115], v[112:113], v[104:105], v[114:115] op_sel:[1,1,0] op_sel_hi:[0,1,1] neg_lo:[1,0,0]
	v_pk_add_f32 v[116:117], v[116:117], v[120:121] neg_lo:[0,1] neg_hi:[0,1]
	v_mov_b64_e32 v[112:113], s[16:17]
	v_pk_mul_f32 v[120:121], v[116:117], v[112:113] op_sel_hi:[1,0]
	v_pk_fma_f32 v[116:117], v[116:117], v[112:113], v[120:121] op_sel:[1,1,0] op_sel_hi:[0,1,1] neg_lo:[1,0,0]
	v_pk_add_f32 v[120:121], v[134:135], v[140:141]
	v_pk_add_f32 v[134:135], v[134:135], v[140:141] neg_lo:[0,1] neg_hi:[0,1]
	v_pk_add_f32 v[140:141], v[136:137], v[142:143]
	v_pk_add_f32 v[136:137], v[136:137], v[142:143] neg_lo:[0,1] neg_hi:[0,1]
	s_nop 0
	v_pk_mul_f32 v[142:143], v[136:137], v[102:103] op_sel_hi:[1,0]
	v_pk_fma_f32 v[136:137], v[136:137], v[102:103], v[142:143] op_sel:[1,1,0] op_sel_hi:[0,1,1] neg_lo:[1,0,0]
	v_pk_add_f32 v[142:143], v[122:123], v[144:145]
	v_pk_add_f32 v[122:123], v[122:123], v[144:145] op_sel:[1,1] op_sel_hi:[0,0] neg_lo:[1,0] neg_hi:[0,1]
	v_pk_add_f32 v[144:145], v[138:139], v[132:133]
	v_pk_add_f32 v[132:133], v[138:139], v[132:133] neg_lo:[0,1] neg_hi:[0,1]
	s_nop 0
	v_pk_mul_f32 v[138:139], v[132:133], v[104:105] op_sel_hi:[1,0]
	v_pk_fma_f32 v[132:133], v[132:133], v[104:105], v[138:139] op_sel:[1,1,0] op_sel_hi:[0,1,1] neg_lo:[1,0,0]
	v_pk_add_f32 v[138:139], v[2:3], v[128:129]
	v_pk_add_f32 v[2:3], v[2:3], v[128:129] neg_lo:[0,1] neg_hi:[0,1]
	v_pk_add_f32 v[128:129], v[4:5], v[130:131]
	v_pk_add_f32 v[4:5], v[4:5], v[130:131] neg_lo:[0,1] neg_hi:[0,1]
	s_nop 0
	v_pk_mul_f32 v[130:131], v[4:5], v[102:103] op_sel_hi:[1,0]
	v_pk_fma_f32 v[4:5], v[4:5], v[102:103], v[130:131] op_sel:[1,1,0] op_sel_hi:[0,1,1] neg_lo:[1,0,0]
	v_pk_add_f32 v[130:131], v[124:125], v[114:115]
	v_pk_add_f32 v[114:115], v[124:125], v[114:115] op_sel:[1,1] op_sel_hi:[0,0] neg_lo:[1,0] neg_hi:[0,1]
	v_pk_add_f32 v[124:125], v[126:127], v[116:117]
	v_pk_add_f32 v[116:117], v[126:127], v[116:117] neg_lo:[0,1] neg_hi:[0,1]
	s_nop 0
	v_pk_mul_f32 v[126:127], v[116:117], v[104:105] op_sel_hi:[1,0]
	v_pk_fma_f32 v[116:117], v[116:117], v[104:105], v[126:127] op_sel:[1,1,0] op_sel_hi:[0,1,1] neg_lo:[1,0,0]
	v_pk_add_f32 v[126:127], v[120:121], v[142:143]
	v_pk_add_f32 v[120:121], v[120:121], v[142:143] neg_lo:[0,1] neg_hi:[0,1]
	v_pk_add_f32 v[142:143], v[140:141], v[144:145]
	v_pk_add_f32 v[140:141], v[140:141], v[144:145] op_sel:[1,1] op_sel_hi:[0,0] neg_lo:[1,0] neg_hi:[0,1]
	v_pk_add_f32 v[144:145], v[134:135], v[122:123]
	v_pk_add_f32 v[122:123], v[134:135], v[122:123] neg_lo:[0,1] neg_hi:[0,1]
	v_pk_add_f32 v[134:135], v[136:137], v[132:133]
	v_pk_add_f32 v[132:133], v[136:137], v[132:133] op_sel:[1,1] op_sel_hi:[0,0] neg_lo:[1,0] neg_hi:[0,1]
	v_pk_add_f32 v[136:137], v[138:139], v[130:131]
	v_pk_add_f32 v[130:131], v[138:139], v[130:131] neg_lo:[0,1] neg_hi:[0,1]
	v_pk_add_f32 v[138:139], v[128:129], v[124:125]
	v_pk_add_f32 v[124:125], v[128:129], v[124:125] op_sel:[1,1] op_sel_hi:[0,0] neg_lo:[1,0] neg_hi:[0,1]
	v_pk_add_f32 v[128:129], v[2:3], v[114:115]
	v_pk_add_f32 v[2:3], v[2:3], v[114:115] neg_lo:[0,1] neg_hi:[0,1]
	v_pk_add_f32 v[114:115], v[4:5], v[116:117]
	v_pk_add_f32 v[4:5], v[4:5], v[116:117] op_sel:[1,1] op_sel_hi:[0,0] neg_lo:[1,0] neg_hi:[0,1]
	v_pk_add_f32 v[116:117], v[126:127], v[142:143]
	v_pk_add_f32 v[2:3], v[2:3], v[4:5]
	s_waitcnt vmcnt(47)
	v_pk_mul_f32 v[4:5], v[38:39], v[116:117] op_sel_hi:[0,1]
	v_lshlrev_b32_e32 v116, 1, v118
	v_ashrrev_i32_e32 v117, 31, v116
	v_pk_add_f32 v[114:115], v[128:129], v[114:115]
	v_lshl_add_u64 v[128:129], v[116:117], 2, s[84:85]
	global_store_dwordx2 v[128:129], v[4:5], off
	v_add_u32_e32 v128, 0x800, v116
	v_pk_add_f32 v[122:123], v[122:123], v[132:133]
	v_pk_add_f32 v[132:133], v[136:137], v[138:139]
	v_ashrrev_i32_e32 v129, 31, v128
	v_pk_add_f32 v[126:127], v[144:145], v[134:135]
	v_pk_mul_f32 v[4:5], v[38:39], v[132:133] op_sel_hi:[0,1]
	v_lshl_add_u64 v[128:129], v[128:129], 2, s[84:85]
	global_store_dwordx2 v[128:129], v[4:5], off
	v_pk_mul_f32 v[4:5], v[38:39], v[126:127] op_sel_hi:[0,1]
	v_add_u32_e32 v126, 0x1000, v116
	v_ashrrev_i32_e32 v127, 31, v126
	v_lshl_add_u64 v[126:127], v[126:127], 2, s[84:85]
	global_store_dwordx2 v[126:127], v[4:5], off
	v_pk_mul_f32 v[4:5], v[38:39], v[114:115] op_sel_hi:[0,1]
	v_add_u32_e32 v114, 0x1800, v116
	v_ashrrev_i32_e32 v115, 31, v114
	v_lshl_add_u64 v[114:115], v[114:115], 2, s[84:85]
	global_store_dwordx2 v[114:115], v[4:5], off
	v_add_u32_e32 v114, 0x2000, v116
	v_pk_add_f32 v[120:121], v[120:121], v[140:141]
	v_ashrrev_i32_e32 v115, 31, v114
	v_pk_mul_f32 v[4:5], v[38:39], v[120:121] op_sel_hi:[0,1]
	v_lshl_add_u64 v[114:115], v[114:115], 2, s[84:85]
	global_store_dwordx2 v[114:115], v[4:5], off
	v_add_u32_e32 v114, 0x2800, v116
	v_pk_add_f32 v[124:125], v[130:131], v[124:125]
	v_ashrrev_i32_e32 v115, 31, v114
	v_pk_mul_f32 v[4:5], v[38:39], v[124:125] op_sel_hi:[0,1]
	v_lshl_add_u64 v[114:115], v[114:115], 2, s[84:85]
	global_store_dwordx2 v[114:115], v[4:5], off
	v_add_u32_e32 v114, 0x3000, v116
	v_ashrrev_i32_e32 v115, 31, v114
	v_pk_mul_f32 v[4:5], v[38:39], v[122:123] op_sel_hi:[0,1]
	v_lshl_add_u64 v[114:115], v[114:115], 2, s[84:85]
	v_add_u32_e32 v130, 0x200, v118
	global_store_dwordx2 v[114:115], v[4:5], off
	v_add_u32_e32 v4, 0x3800, v116
	v_cvt_f32_i32_e32 v114, v130
	v_ashrrev_i32_e32 v5, 31, v4
	v_pk_mul_f32 v[2:3], v[38:39], v[2:3] op_sel_hi:[0,1]
	v_lshl_add_u64 v[4:5], v[4:5], 2, s[84:85]
	global_store_dwordx2 v[4:5], v[2:3], off
	v_and_b32_e32 v2, -8, v130
	v_add3_u32 v128, 0, v2, v119
	v_mul_f32_e32 v114, 0x38800000, v114
	ds_read2st64_b64 v[2:5], v128 offset0:8 offset1:26
	v_cos_f32_e32 v118, v114
	v_sin_f32_e32 v119, v114
	s_waitcnt lgkmcnt(0)
	v_pk_mul_f32 v[114:115], v[4:5], v[118:119] op_sel_hi:[1,0]
	ds_read2st64_b64 v[120:123], v128 offset0:44 offset1:62
	v_pk_fma_f32 v[4:5], v[4:5], v[118:119], v[114:115] op_sel:[1,1,0] op_sel_hi:[0,1,1] neg_lo:[1,0,0]
	v_pk_mul_f32 v[114:115], v[118:119], v[118:119] op_sel_hi:[1,0]
	v_add_u32_e32 v131, 0x1000, v128
	v_pk_fma_f32 v[114:115], v[118:119], v[118:119], v[114:115] op_sel:[1,1,0] op_sel_hi:[0,1,1] neg_lo:[1,0,0]
	v_add_u32_e32 v134, 0x13000, v128
	s_waitcnt lgkmcnt(0)
	ds_read2st64_b64 v[230:233], v128 offset0:80 offset1:98
	v_pk_mul_f32 v[116:117], v[120:121], v[114:115] op_sel_hi:[1,0]
	v_add_u32_e32 v136, 0x15400, v128
	v_pk_fma_f32 v[116:117], v[120:121], v[114:115], v[116:117] op_sel:[1,1,0] op_sel_hi:[0,1,1] neg_lo:[1,0,0]
	v_pk_mul_f32 v[120:121], v[114:115], v[118:119] op_sel_hi:[1,0]
	v_add_u32_e32 v138, 0x17800, v128
	v_pk_fma_f32 v[120:121], v[114:115], v[118:119], v[120:121] op_sel:[1,1,0] op_sel_hi:[0,1,1] neg_lo:[1,0,0]
	v_add_u32_e32 v140, 0x19c00, v128
	v_pk_mul_f32 v[114:115], v[122:123], v[120:121] op_sel_hi:[1,0]
	v_add_u32_e32 v142, 0x1c000, v128
	v_pk_fma_f32 v[114:115], v[122:123], v[120:121], v[114:115] op_sel:[1,1,0] op_sel_hi:[0,1,1] neg_lo:[1,0,0]
	v_pk_mul_f32 v[122:123], v[120:121], v[118:119] op_sel_hi:[1,0]
	v_add_u32_e32 v144, 0x1e400, v128
	v_pk_fma_f32 v[124:125], v[120:121], v[118:119], v[122:123] op_sel:[1,1,0] op_sel_hi:[0,1,1] neg_lo:[1,0,0]
	s_waitcnt lgkmcnt(0)
	ds_read_b64 v[234:235], v128 offset:59392
	v_pk_mul_f32 v[126:127], v[230:231], v[124:125] op_sel_hi:[1,0]
	v_add_u32_e32 v146, 0x20800, v128
	v_pk_fma_f32 v[120:121], v[230:231], v[124:125], v[126:127] op_sel:[1,1,0] op_sel_hi:[0,1,1] neg_lo:[1,0,0]
	v_pk_mul_f32 v[126:127], v[124:125], v[118:119] op_sel_hi:[1,0]
	v_add_u32_e32 v148, 0x22c00, v128
	v_pk_fma_f32 v[124:125], v[124:125], v[118:119], v[126:127] op_sel:[1,1,0] op_sel_hi:[0,1,1] neg_lo:[1,0,0]
	v_pk_mul_f32 v[126:127], v[232:233], v[124:125] op_sel_hi:[1,0]
	v_pk_fma_f32 v[122:123], v[232:233], v[124:125], v[126:127] op_sel:[1,1,0] op_sel_hi:[0,1,1] neg_lo:[1,0,0]
	v_pk_mul_f32 v[126:127], v[124:125], v[118:119] op_sel_hi:[1,0]
	v_pk_fma_f32 v[126:127], v[124:125], v[118:119], v[126:127] op_sel:[1,1,0] op_sel_hi:[0,1,1] neg_lo:[1,0,0]
	s_waitcnt lgkmcnt(0)
	ds_read_b64 v[230:231], v131 offset:64512
	v_pk_mul_f32 v[128:129], v[234:235], v[126:127] op_sel_hi:[1,0]
	v_pk_fma_f32 v[124:125], v[234:235], v[126:127], v[128:129] op_sel:[1,1,0] op_sel_hi:[0,1,1] neg_lo:[1,0,0]
	v_pk_mul_f32 v[128:129], v[126:127], v[118:119] op_sel_hi:[1,0]
	v_pk_fma_f32 v[128:129], v[126:127], v[118:119], v[128:129] op_sel:[1,1,0] op_sel_hi:[0,1,1] neg_lo:[1,0,0]
	s_waitcnt lgkmcnt(0)
	ds_read_b64 v[232:233], v134
	v_pk_mul_f32 v[132:133], v[230:231], v[128:129] op_sel_hi:[1,0]
	v_pk_fma_f32 v[126:127], v[230:231], v[128:129], v[132:133] op_sel:[1,1,0] op_sel_hi:[0,1,1] neg_lo:[1,0,0]
	v_pk_mul_f32 v[132:133], v[128:129], v[118:119] op_sel_hi:[1,0]
	v_pk_fma_f32 v[132:133], v[128:129], v[118:119], v[132:133] op_sel:[1,1,0] op_sel_hi:[0,1,1] neg_lo:[1,0,0]
	s_waitcnt lgkmcnt(0)
	ds_read_b64 v[230:231], v136
	v_pk_mul_f32 v[134:135], v[232:233], v[132:133] op_sel_hi:[1,0]
	v_pk_fma_f32 v[128:129], v[232:233], v[132:133], v[134:135] op_sel:[1,1,0] op_sel_hi:[0,1,1] neg_lo:[1,0,0]
	v_pk_mul_f32 v[134:135], v[132:133], v[118:119] op_sel_hi:[1,0]
	v_pk_fma_f32 v[132:133], v[132:133], v[118:119], v[134:135] op_sel:[1,1,0] op_sel_hi:[0,1,1] neg_lo:[1,0,0]
	s_waitcnt lgkmcnt(0)
	ds_read_b64 v[232:233], v138
	v_pk_mul_f32 v[136:137], v[230:231], v[132:133] op_sel_hi:[1,0]
	v_pk_fma_f32 v[134:135], v[230:231], v[132:133], v[136:137] op_sel:[1,1,0] op_sel_hi:[0,1,1] neg_lo:[1,0,0]
	v_pk_mul_f32 v[136:137], v[132:133], v[118:119] op_sel_hi:[1,0]
	v_pk_fma_f32 v[132:133], v[132:133], v[118:119], v[136:137] op_sel:[1,1,0] op_sel_hi:[0,1,1] neg_lo:[1,0,0]
	s_waitcnt lgkmcnt(0)
	ds_read_b64 v[230:231], v140
	v_pk_mul_f32 v[138:139], v[232:233], v[132:133] op_sel_hi:[1,0]
	v_pk_fma_f32 v[136:137], v[232:233], v[132:133], v[138:139] op_sel:[1,1,0] op_sel_hi:[0,1,1] neg_lo:[1,0,0]
	v_pk_mul_f32 v[138:139], v[132:133], v[118:119] op_sel_hi:[1,0]
	v_pk_fma_f32 v[132:133], v[132:133], v[118:119], v[138:139] op_sel:[1,1,0] op_sel_hi:[0,1,1] neg_lo:[1,0,0]
	s_waitcnt lgkmcnt(0)
	ds_read_b64 v[232:233], v142
	v_pk_mul_f32 v[140:141], v[230:231], v[132:133] op_sel_hi:[1,0]
	v_pk_fma_f32 v[138:139], v[230:231], v[132:133], v[140:141] op_sel:[1,1,0] op_sel_hi:[0,1,1] neg_lo:[1,0,0]
	v_pk_mul_f32 v[140:141], v[132:133], v[118:119] op_sel_hi:[1,0]
	v_pk_fma_f32 v[132:133], v[132:133], v[118:119], v[140:141] op_sel:[1,1,0] op_sel_hi:[0,1,1] neg_lo:[1,0,0]
	s_waitcnt lgkmcnt(0)
	ds_read_b64 v[230:231], v144
	v_pk_mul_f32 v[142:143], v[232:233], v[132:133] op_sel_hi:[1,0]
	v_pk_fma_f32 v[140:141], v[232:233], v[132:133], v[142:143] op_sel:[1,1,0] op_sel_hi:[0,1,1] neg_lo:[1,0,0]
	v_pk_mul_f32 v[142:143], v[132:133], v[118:119] op_sel_hi:[1,0]
	v_pk_fma_f32 v[132:133], v[132:133], v[118:119], v[142:143] op_sel:[1,1,0] op_sel_hi:[0,1,1] neg_lo:[1,0,0]
	s_waitcnt lgkmcnt(0)
	ds_read_b64 v[232:233], v146
	v_pk_mul_f32 v[144:145], v[230:231], v[132:133] op_sel_hi:[1,0]
	v_pk_fma_f32 v[142:143], v[230:231], v[132:133], v[144:145] op_sel:[1,1,0] op_sel_hi:[0,1,1] neg_lo:[1,0,0]
	v_pk_mul_f32 v[144:145], v[132:133], v[118:119] op_sel_hi:[1,0]
	v_pk_fma_f32 v[132:133], v[132:133], v[118:119], v[144:145] op_sel:[1,1,0] op_sel_hi:[0,1,1] neg_lo:[1,0,0]
	s_waitcnt lgkmcnt(0)
	v_pk_mul_f32 v[146:147], v[232:233], v[132:133] op_sel_hi:[1,0]
	v_pk_fma_f32 v[144:145], v[232:233], v[132:133], v[146:147] op_sel:[1,1,0] op_sel_hi:[0,1,1] neg_lo:[1,0,0]
	v_pk_mul_f32 v[146:147], v[132:133], v[118:119] op_sel_hi:[1,0]
	v_pk_fma_f32 v[118:119], v[132:133], v[118:119], v[146:147] op_sel:[1,1,0] op_sel_hi:[0,1,1] neg_lo:[1,0,0]
	ds_read_b64 v[132:133], v148
	s_waitcnt lgkmcnt(0)
	v_pk_mul_f32 v[146:147], v[132:133], v[118:119] op_sel_hi:[1,0]
	v_pk_fma_f32 v[118:119], v[132:133], v[118:119], v[146:147] op_sel:[1,1,0] op_sel_hi:[0,1,1] neg_lo:[1,0,0]
	v_pk_add_f32 v[132:133], v[2:3], v[128:129]
	v_pk_add_f32 v[2:3], v[2:3], v[128:129] neg_lo:[0,1] neg_hi:[0,1]
	v_pk_add_f32 v[128:129], v[4:5], v[134:135]
	v_pk_add_f32 v[4:5], v[4:5], v[134:135] neg_lo:[0,1] neg_hi:[0,1]
	s_nop 0
	v_pk_mul_f32 v[134:135], v[4:5], v[106:107] op_sel_hi:[1,0]
	v_pk_fma_f32 v[4:5], v[4:5], v[106:107], v[134:135] op_sel:[1,1,0] op_sel_hi:[0,1,1] neg_lo:[1,0,0]
	v_pk_add_f32 v[106:107], v[116:117], v[136:137]
	v_pk_add_f32 v[116:117], v[116:117], v[136:137] neg_lo:[0,1] neg_hi:[0,1]
	s_nop 0
	v_pk_mul_f32 v[134:135], v[116:117], v[102:103] op_sel_hi:[1,0]
	v_pk_fma_f32 v[116:117], v[116:117], v[102:103], v[134:135] op_sel:[1,1,0] op_sel_hi:[0,1,1] neg_lo:[1,0,0]
	v_pk_add_f32 v[134:135], v[114:115], v[138:139]
	v_pk_add_f32 v[114:115], v[114:115], v[138:139] neg_lo:[0,1] neg_hi:[0,1]
	s_nop 0
	v_pk_mul_f32 v[136:137], v[114:115], v[108:109] op_sel_hi:[1,0]
	v_pk_fma_f32 v[108:109], v[114:115], v[108:109], v[136:137] op_sel:[1,1,0] op_sel_hi:[0,1,1] neg_lo:[1,0,0]
	v_pk_add_f32 v[136:137], v[122:123], v[142:143]
	v_pk_add_f32 v[122:123], v[122:123], v[142:143] neg_lo:[0,1] neg_hi:[0,1]
	v_pk_add_f32 v[114:115], v[120:121], v[140:141]
	v_pk_mul_f32 v[138:139], v[122:123], v[110:111] op_sel_hi:[1,0]
	v_pk_add_f32 v[120:121], v[120:121], v[140:141] op_sel:[1,1] op_sel_hi:[0,0] neg_lo:[1,0] neg_hi:[0,1]
	v_pk_fma_f32 v[110:111], v[122:123], v[110:111], v[138:139] op_sel:[1,1,0] op_sel_hi:[0,1,1] neg_lo:[1,0,0]
	v_pk_add_f32 v[122:123], v[124:125], v[144:145]
	v_pk_add_f32 v[124:125], v[124:125], v[144:145] neg_lo:[0,1] neg_hi:[0,1]
	s_nop 0
	v_pk_mul_f32 v[138:139], v[124:125], v[104:105] op_sel_hi:[1,0]
	v_pk_fma_f32 v[124:125], v[124:125], v[104:105], v[138:139] op_sel:[1,1,0] op_sel_hi:[0,1,1] neg_lo:[1,0,0]
	v_pk_add_f32 v[138:139], v[126:127], v[118:119]
	v_pk_add_f32 v[118:119], v[126:127], v[118:119] neg_lo:[0,1] neg_hi:[0,1]
	s_nop 0
	v_pk_mul_f32 v[126:127], v[118:119], v[112:113] op_sel_hi:[1,0]
	v_pk_fma_f32 v[112:113], v[118:119], v[112:113], v[126:127] op_sel:[1,1,0] op_sel_hi:[0,1,1] neg_lo:[1,0,0]
	v_pk_add_f32 v[118:119], v[132:133], v[114:115]
	v_pk_add_f32 v[114:115], v[132:133], v[114:115] neg_lo:[0,1] neg_hi:[0,1]
	v_pk_add_f32 v[126:127], v[128:129], v[136:137]
	v_pk_add_f32 v[128:129], v[128:129], v[136:137] neg_lo:[0,1] neg_hi:[0,1]
	s_nop 0
	v_pk_mul_f32 v[132:133], v[128:129], v[102:103] op_sel_hi:[1,0]
	v_pk_fma_f32 v[128:129], v[128:129], v[102:103], v[132:133] op_sel:[1,1,0] op_sel_hi:[0,1,1] neg_lo:[1,0,0]
	v_pk_add_f32 v[132:133], v[106:107], v[122:123]
	v_pk_add_f32 v[106:107], v[106:107], v[122:123] op_sel:[1,1] op_sel_hi:[0,0] neg_lo:[1,0] neg_hi:[0,1]
	v_pk_add_f32 v[122:123], v[134:135], v[138:139]
	v_pk_add_f32 v[134:135], v[134:135], v[138:139] neg_lo:[0,1] neg_hi:[0,1]
	s_nop 0
	v_pk_mul_f32 v[136:137], v[134:135], v[104:105] op_sel_hi:[1,0]
	v_pk_fma_f32 v[134:135], v[134:135], v[104:105], v[136:137] op_sel:[1,1,0] op_sel_hi:[0,1,1] neg_lo:[1,0,0]
	v_pk_add_f32 v[136:137], v[2:3], v[120:121]
	v_pk_add_f32 v[2:3], v[2:3], v[120:121] neg_lo:[0,1] neg_hi:[0,1]
	v_pk_add_f32 v[120:121], v[4:5], v[110:111]
	v_pk_add_f32 v[4:5], v[4:5], v[110:111] neg_lo:[0,1] neg_hi:[0,1]
	s_nop 0
	v_pk_mul_f32 v[110:111], v[4:5], v[102:103] op_sel_hi:[1,0]
	v_pk_fma_f32 v[4:5], v[4:5], v[102:103], v[110:111] op_sel:[1,1,0] op_sel_hi:[0,1,1] neg_lo:[1,0,0]
	v_pk_add_f32 v[102:103], v[116:117], v[124:125]
	v_pk_add_f32 v[110:111], v[116:117], v[124:125] op_sel:[1,1] op_sel_hi:[0,0] neg_lo:[1,0] neg_hi:[0,1]
	v_pk_add_f32 v[116:117], v[108:109], v[112:113]
	v_pk_add_f32 v[108:109], v[108:109], v[112:113] neg_lo:[0,1] neg_hi:[0,1]
	v_pk_add_f32 v[124:125], v[114:115], v[106:107]
	v_pk_mul_f32 v[112:113], v[108:109], v[104:105] op_sel_hi:[1,0]
	v_pk_add_f32 v[106:107], v[114:115], v[106:107] neg_lo:[0,1] neg_hi:[0,1]
	v_pk_fma_f32 v[104:105], v[108:109], v[104:105], v[112:113] op_sel:[1,1,0] op_sel_hi:[0,1,1] neg_lo:[1,0,0]
	v_pk_add_f32 v[108:109], v[118:119], v[132:133]
	v_pk_add_f32 v[112:113], v[118:119], v[132:133] neg_lo:[0,1] neg_hi:[0,1]
	v_pk_add_f32 v[118:119], v[126:127], v[122:123]
	v_pk_add_f32 v[132:133], v[120:121], v[116:117]
	v_pk_add_f32 v[116:117], v[120:121], v[116:117] op_sel:[1,1] op_sel_hi:[0,0] neg_lo:[1,0] neg_hi:[0,1]
	v_pk_add_f32 v[120:121], v[2:3], v[110:111]
	v_pk_add_f32 v[2:3], v[2:3], v[110:111] neg_lo:[0,1] neg_hi:[0,1]
	v_pk_add_f32 v[110:111], v[4:5], v[104:105]
	v_pk_add_f32 v[4:5], v[4:5], v[104:105] op_sel:[1,1] op_sel_hi:[0,0] neg_lo:[1,0] neg_hi:[0,1]
	v_pk_add_f32 v[104:105], v[108:109], v[118:119]
	v_pk_add_f32 v[2:3], v[2:3], v[4:5]
	v_pk_mul_f32 v[4:5], v[38:39], v[104:105] op_sel_hi:[0,1]
	v_lshlrev_b32_e32 v104, 1, v130
	v_pk_add_f32 v[122:123], v[126:127], v[122:123] op_sel:[1,1] op_sel_hi:[0,0] neg_lo:[1,0] neg_hi:[0,1]
	v_pk_add_f32 v[114:115], v[128:129], v[134:135]
	v_pk_add_f32 v[126:127], v[128:129], v[134:135] op_sel:[1,1] op_sel_hi:[0,0] neg_lo:[1,0] neg_hi:[0,1]
	v_pk_add_f32 v[128:129], v[136:137], v[102:103]
	v_pk_add_f32 v[102:103], v[136:137], v[102:103] neg_lo:[0,1] neg_hi:[0,1]
	v_ashrrev_i32_e32 v105, 31, v104
	v_pk_add_f32 v[108:109], v[112:113], v[122:123]
	v_pk_add_f32 v[112:113], v[124:125], v[114:115]
	v_pk_add_f32 v[114:115], v[128:129], v[132:133]
	v_pk_add_f32 v[102:103], v[102:103], v[116:117]
	v_lshl_add_u64 v[116:117], v[104:105], 2, s[84:85]
	global_store_dwordx2 v[116:117], v[4:5], off
	v_pk_mul_f32 v[4:5], v[38:39], v[114:115] op_sel_hi:[0,1]
	v_add_u32_e32 v114, 0x800, v104
	v_ashrrev_i32_e32 v115, 31, v114
	v_lshl_add_u64 v[114:115], v[114:115], 2, s[84:85]
	global_store_dwordx2 v[114:115], v[4:5], off
	v_pk_mul_f32 v[4:5], v[38:39], v[112:113] op_sel_hi:[0,1]
	v_add_u32_e32 v112, 0x1000, v104
	v_ashrrev_i32_e32 v113, 31, v112
	v_pk_add_f32 v[110:111], v[120:121], v[110:111]
	v_lshl_add_u64 v[112:113], v[112:113], 2, s[84:85]
	global_store_dwordx2 v[112:113], v[4:5], off
	v_pk_mul_f32 v[4:5], v[38:39], v[110:111] op_sel_hi:[0,1]
	v_add_u32_e32 v110, 0x1800, v104
	v_ashrrev_i32_e32 v111, 31, v110
	v_lshl_add_u64 v[110:111], v[110:111], 2, s[84:85]
	global_store_dwordx2 v[110:111], v[4:5], off
	v_pk_mul_f32 v[4:5], v[38:39], v[108:109] op_sel_hi:[0,1]
	v_add_u32_e32 v108, 0x2000, v104
	v_ashrrev_i32_e32 v109, 31, v108
	v_lshl_add_u64 v[108:109], v[108:109], 2, s[84:85]
	global_store_dwordx2 v[108:109], v[4:5], off
	v_pk_mul_f32 v[4:5], v[38:39], v[102:103] op_sel_hi:[0,1]
	v_add_u32_e32 v102, 0x2800, v104
	v_ashrrev_i32_e32 v103, 31, v102
	v_lshl_add_u64 v[102:103], v[102:103], 2, s[84:85]
	global_store_dwordx2 v[102:103], v[4:5], off
	v_add_u32_e32 v102, 0x3000, v104
	v_pk_add_f32 v[106:107], v[106:107], v[126:127]
	v_ashrrev_i32_e32 v103, 31, v102
	v_pk_mul_f32 v[4:5], v[38:39], v[106:107] op_sel_hi:[0,1]
	v_lshl_add_u64 v[102:103], v[102:103], 2, s[84:85]
	global_store_dwordx2 v[102:103], v[4:5], off
	v_add_u32_e32 v4, 0x3800, v104
	v_ashrrev_i32_e32 v5, 31, v4
	v_pk_mul_f32 v[2:3], v[38:39], v[2:3] op_sel_hi:[0,1]
	v_lshl_add_u64 v[4:5], v[4:5], 2, s[84:85]
	global_store_dwordx2 v[4:5], v[2:3], off
	s_waitcnt lgkmcnt(0)
	s_barrier
	s_cbranch_scc1 .LBB0_755
	v_readlane_b32 s86, v253, 12
	s_add_i32 s95, s95, s86
	s_cmpk_lt_i32 s95, 0x100
	s_barrier
	v_readlane_b32 s87, v253, 13
	s_cbranch_scc1 .LBB0_750
	v_readlane_b32 s88, v253, 16
	v_readlane_b32 s84, v253, 31
	v_readlane_b32 s92, v253, 20
	v_readlane_b32 s60, v252, 57
	v_readlane_b32 s64, v252, 41
	v_readlane_b32 s36, v253, 14
	v_readlane_b32 s94, v253, 22
	v_readlane_b32 s95, v253, 23
	s_mov_b32 s92, s84
	v_readlane_b32 s97, v253, 28
	v_readlane_b32 s63, v253, 27
	v_readlane_b32 s61, v252, 58
	v_readlane_b32 s56, v252, 59
	v_readlane_b32 s72, v252, 49
	v_readlane_b32 s73, v252, 50
	s_mov_b32 s62, s86
	v_readlane_b32 s37, v253, 15
	v_readlane_b32 s85, v253, 32
	v_readlane_b32 s89, v253, 17
	v_readlane_b32 s90, v253, 18
	v_readlane_b32 s91, v253, 19
	v_readlane_b32 s93, v253, 21
	v_readlane_b32 s65, v252, 42
	v_readlane_b32 s66, v252, 43
	v_readlane_b32 s67, v252, 44
	v_readlane_b32 s68, v252, 45
	v_readlane_b32 s69, v252, 46
	v_readlane_b32 s70, v252, 47
	v_readlane_b32 s71, v252, 48
	v_readlane_b32 s74, v252, 51
	v_readlane_b32 s75, v252, 52
	v_readlane_b32 s76, v252, 53
	v_readlane_b32 s77, v252, 54
	v_readlane_b32 s78, v252, 55
	v_readlane_b32 s79, v252, 56
